# attention KV loops (GQA, MLA, NA): second score MFMA takes the shared C tile as srcC directly; 8 v_mov_b64 accumulator-init copies per KV tile removed, on top of v062
# speedup vs baseline: 1.0005x; 1.0005x over previous
.LBB0_376:
	s_waitcnt lgkmcnt(0)
	s_barrier
	ds_read_b128 v[98:101], v191 offset:0
	ds_read_b128 v[102:105], v191 offset:16
	ds_read_b128 v[114:117], v191 offset:64
	ds_read_b128 v[118:121], v191 offset:0x50
	ds_read_b128 v[154:157], v191 offset:0x1200
	ds_read_b128 v[158:161], v191 offset:0x1210
	ds_read_b128 v[162:165], v191 offset:0x1240
	ds_read_b128 v[166:169], v191 offset:0x1250
	s_nop 0
	s_waitcnt lgkmcnt(6)
	s_nop 0
	v_mfma_scale_f32_32x32x64_f8f6f4 v[98:113], v[98:105], v[138:145], v[82:97], v195, v194 op_sel_hi:[0,0,0]
	s_waitcnt lgkmcnt(4)
	s_waitcnt lgkmcnt(2)
	s_waitcnt lgkmcnt(0)
	s_nop 0
	v_mfma_scale_f32_32x32x64_f8f6f4 v[98:113], v[114:121], v[146:153], v[98:113], v195, v194 op_sel_hi:[0,0,0]
	v_mfma_scale_f32_32x32x64_f8f6f4 v[114:129], v[154:161], v[138:145], v[82:97], v195, v194 op_sel_hi:[0,0,0]
	s_nop 15
	s_nop 2
	v_max3_f32 v131, v98, s26, v99
	v_max3_f32 v131, v131, v100, v101
	v_max3_f32 v131, v131, v102, v103
	v_max3_f32 v131, v131, v104, v105
	v_max3_f32 v131, v131, v106, v107
	v_max3_f32 v131, v131, v108, v109
	v_max3_f32 v131, v131, v110, v111
	v_max3_f32 v131, v131, v112, v113
	v_mfma_scale_f32_32x32x64_f8f6f4 v[114:129], v[162:169], v[146:153], v[114:129], v195, v194 op_sel_hi:[0,0,0]
	ds_read_b64_tr_b8 v[162:163], v190 offset:0
	ds_read_b64_tr_b8 v[164:165], v190 offset:0x900
	ds_read_b64_tr_b8 v[166:167], v190 offset:0x1200
	ds_read_b64_tr_b8 v[168:169], v190 offset:0x1b00
	ds_read_b64_tr_b8 v[154:155], v190 offset:32
	ds_read_b64_tr_b8 v[156:157], v190 offset:0x920
	ds_read_b64_tr_b8 v[158:159], v190 offset:0x1220
	ds_read_b64_tr_b8 v[160:161], v190 offset:0x1b20
	s_nop 15
	s_nop 3
	v_max3_f32 v131, v131, v114, v115
	v_max3_f32 v131, v131, v116, v117
	v_max3_f32 v131, v131, v118, v119
	v_max3_f32 v131, v131, v120, v121
	v_max3_f32 v131, v131, v122, v123
	v_max3_f32 v131, v131, v124, v125
	v_max3_f32 v131, v131, v126, v127
	v_max3_f32 v131, v131, v128, v129
	ds_bpermute_b32 v132, v199, v131
	s_waitcnt lgkmcnt(0)
	v_max_f32_e32 v132, v132, v132
	v_max_f32_e32 v131, v131, v132
	v_cmp_lt_f32_e32 vcc, s27, v131
	s_cbranch_vccz .LBB0_378
	v_add_f32_e32 v83, -4.0, v131
	v_max_f32_e32 v84, 0, v83
	v_exp_f32_e64 v86, -v84
	v_sub_f32_e32 v82, v82, v84
	v_pk_add_f32 v[98:99], v[98:99], v[84:85] op_sel_hi:[1,0] neg_lo:[0,1] neg_hi:[0,1]
	v_pk_add_f32 v[100:101], v[100:101], v[84:85] op_sel_hi:[1,0] neg_lo:[0,1] neg_hi:[0,1]
	v_pk_mul_f32 v[48:49], v[48:49], v[86:87] op_sel_hi:[1,0]
	v_pk_mul_f32 v[46:47], v[46:47], v[86:87] op_sel_hi:[1,0]
	v_pk_mul_f32 v[44:45], v[44:45], v[86:87] op_sel_hi:[1,0]
	v_pk_mul_f32 v[42:43], v[42:43], v[86:87] op_sel_hi:[1,0]
	v_pk_mul_f32 v[40:41], v[40:41], v[86:87] op_sel_hi:[1,0]
	v_pk_mul_f32 v[38:39], v[38:39], v[86:87] op_sel_hi:[1,0]
	v_pk_mul_f32 v[36:37], v[36:37], v[86:87] op_sel_hi:[1,0]
	v_pk_mul_f32 v[34:35], v[34:35], v[86:87] op_sel_hi:[1,0]
	v_pk_mul_f32 v[80:81], v[80:81], v[86:87] op_sel_hi:[1,0]
	v_pk_mul_f32 v[78:79], v[78:79], v[86:87] op_sel_hi:[1,0]
	v_pk_mul_f32 v[76:77], v[76:77], v[86:87] op_sel_hi:[1,0]
	v_pk_mul_f32 v[74:75], v[74:75], v[86:87] op_sel_hi:[1,0]
	v_pk_mul_f32 v[72:73], v[72:73], v[86:87] op_sel_hi:[1,0]
	v_pk_mul_f32 v[70:71], v[70:71], v[86:87] op_sel_hi:[1,0]
	v_pk_mul_f32 v[68:69], v[68:69], v[86:87] op_sel_hi:[1,0]
	v_pk_mul_f32 v[66:67], v[66:67], v[86:87] op_sel_hi:[1,0]
	v_pk_mul_f32 v[64:65], v[64:65], v[86:87] op_sel_hi:[1,0]
	v_pk_mul_f32 v[62:63], v[62:63], v[86:87] op_sel_hi:[1,0]
	v_pk_mul_f32 v[60:61], v[60:61], v[86:87] op_sel_hi:[1,0]
	v_pk_mul_f32 v[58:59], v[58:59], v[86:87] op_sel_hi:[1,0]
	v_pk_mul_f32 v[56:57], v[56:57], v[86:87] op_sel_hi:[1,0]
	v_pk_mul_f32 v[54:55], v[54:55], v[86:87] op_sel_hi:[1,0]
	v_pk_mul_f32 v[52:53], v[52:53], v[86:87] op_sel_hi:[1,0]
	v_pk_mul_f32 v[50:51], v[50:51], v[86:87] op_sel_hi:[1,0]
	v_pk_mul_f32 v[32:33], v[32:33], v[86:87] op_sel_hi:[1,0]
	v_pk_mul_f32 v[30:31], v[30:31], v[86:87] op_sel_hi:[1,0]
	v_pk_mul_f32 v[28:29], v[28:29], v[86:87] op_sel_hi:[1,0]
	v_pk_mul_f32 v[26:27], v[26:27], v[86:87] op_sel_hi:[1,0]
	v_pk_mul_f32 v[24:25], v[24:25], v[86:87] op_sel_hi:[1,0]
	v_pk_mul_f32 v[22:23], v[22:23], v[86:87] op_sel_hi:[1,0]
	v_pk_mul_f32 v[20:21], v[20:21], v[86:87] op_sel_hi:[1,0]
	v_pk_mul_f32 v[18:19], v[18:19], v[86:87] op_sel_hi:[1,0]
	v_pk_mul_f32 v[16:17], v[16:17], v[86:87] op_sel_hi:[1,0]
	v_pk_mul_f32 v[14:15], v[14:15], v[86:87] op_sel_hi:[1,0]
	v_pk_mul_f32 v[12:13], v[12:13], v[86:87] op_sel_hi:[1,0]
	v_pk_mul_f32 v[10:11], v[10:11], v[86:87] op_sel_hi:[1,0]
	v_pk_mul_f32 v[8:9], v[8:9], v[86:87] op_sel_hi:[1,0]
	v_pk_mul_f32 v[6:7], v[6:7], v[86:87] op_sel_hi:[1,0]
	v_pk_mul_f32 v[4:5], v[4:5], v[86:87] op_sel_hi:[1,0]
	v_pk_mul_f32 v[2:3], v[2:3], v[86:87] op_sel_hi:[1,0]
	v_pk_add_f32 v[102:103], v[102:103], v[84:85] op_sel_hi:[1,0] neg_lo:[0,1] neg_hi:[0,1]
	v_pk_add_f32 v[104:105], v[104:105], v[84:85] op_sel_hi:[1,0] neg_lo:[0,1] neg_hi:[0,1]
	v_pk_add_f32 v[106:107], v[106:107], v[84:85] op_sel_hi:[1,0] neg_lo:[0,1] neg_hi:[0,1]
	v_pk_add_f32 v[108:109], v[108:109], v[84:85] op_sel_hi:[1,0] neg_lo:[0,1] neg_hi:[0,1]
	v_pk_add_f32 v[110:111], v[110:111], v[84:85] op_sel_hi:[1,0] neg_lo:[0,1] neg_hi:[0,1]
	v_pk_add_f32 v[112:113], v[112:113], v[84:85] op_sel_hi:[1,0] neg_lo:[0,1] neg_hi:[0,1]
	v_pk_add_f32 v[114:115], v[114:115], v[84:85] op_sel_hi:[1,0] neg_lo:[0,1] neg_hi:[0,1]
	v_pk_add_f32 v[116:117], v[116:117], v[84:85] op_sel_hi:[1,0] neg_lo:[0,1] neg_hi:[0,1]
	v_pk_add_f32 v[118:119], v[118:119], v[84:85] op_sel_hi:[1,0] neg_lo:[0,1] neg_hi:[0,1]
	v_pk_add_f32 v[120:121], v[120:121], v[84:85] op_sel_hi:[1,0] neg_lo:[0,1] neg_hi:[0,1]
	v_pk_add_f32 v[122:123], v[122:123], v[84:85] op_sel_hi:[1,0] neg_lo:[0,1] neg_hi:[0,1]
	v_pk_add_f32 v[124:125], v[124:125], v[84:85] op_sel_hi:[1,0] neg_lo:[0,1] neg_hi:[0,1]
	v_pk_add_f32 v[126:127], v[126:127], v[84:85] op_sel_hi:[1,0] neg_lo:[0,1] neg_hi:[0,1]
	v_pk_add_f32 v[128:129], v[128:129], v[84:85] op_sel_hi:[1,0] neg_lo:[0,1] neg_hi:[0,1]
	v_mov_b32_e32 v83, v82
	v_mov_b32_e32 v84, v82
	v_mov_b32_e32 v85, v82
	v_mov_b32_e32 v86, v82
	v_mov_b32_e32 v87, v82
	v_mov_b32_e32 v88, v82
	v_mov_b32_e32 v89, v82
	v_mov_b32_e32 v90, v82
	v_mov_b32_e32 v91, v82
	v_mov_b32_e32 v92, v82
	v_mov_b32_e32 v93, v82
	v_mov_b32_e32 v94, v82
	v_mov_b32_e32 v95, v82
	v_mov_b32_e32 v96, v82
	v_mov_b32_e32 v97, v82

.LBB0_1051:
	s_waitcnt lgkmcnt(0)
	s_barrier
	ds_read_b128 v[82:85], v202 offset:0
	ds_read_b128 v[86:89], v202 offset:16
	ds_read_b128 v[98:101], v202 offset:64
	ds_read_b128 v[102:105], v202 offset:0x50
	ds_read_b128 v[106:109], v202 offset:0x80
	ds_read_b128 v[110:113], v202 offset:0x90
	ds_read_b128 v[138:141], v202 offset:0x1a00
	ds_read_b128 v[142:145], v202 offset:0x1a10
	s_nop 0
	s_waitcnt lgkmcnt(6)
	s_nop 0
	v_mfma_scale_f32_32x32x64_f8f6f4 v[82:97], v[82:89], v[114:121], v[66:81], v219, v218 op_sel_hi:[0,0,0]
	ds_read_b128 v[146:149], v202 offset:0x1a40
	ds_read_b128 v[150:153], v202 offset:0x1a50
	s_waitcnt lgkmcnt(6)
	ds_read_b128 v[228:231], v202 offset:0x1a80
	ds_read_b128 v[232:235], v202 offset:0x1a90
	s_waitcnt lgkmcnt(6)
	s_waitcnt lgkmcnt(4)
	s_nop 0
	s_waitcnt lgkmcnt(2)
	s_waitcnt lgkmcnt(0)
	v_mfma_scale_f32_32x32x64_f8f6f4 v[82:97], v[98:105], v[122:129], v[82:97], v219, v218 op_sel_hi:[0,0,0]
	v_mfma_scale_f32_32x32x64_f8f6f4 v[82:97], v[106:113], v[130:137], v[82:97], v219, v218 op_sel_hi:[0,0,0]
	v_mfma_scale_f32_32x32x64_f8f6f4 v[98:113], v[138:145], v[114:121], v[66:81], v219, v218 op_sel_hi:[0,0,0]
	s_nop 15
	s_nop 2
	v_max3_f32 v138, v82, s35, v83
	v_max3_f32 v138, v138, v84, v85
	v_max3_f32 v138, v138, v86, v87
	v_max3_f32 v138, v138, v88, v89
	v_max3_f32 v138, v138, v90, v91
	v_max3_f32 v138, v138, v92, v93
	v_max3_f32 v138, v138, v94, v95
	v_max3_f32 v138, v138, v96, v97
	v_mfma_scale_f32_32x32x64_f8f6f4 v[98:113], v[146:153], v[122:129], v[98:113], v219, v218 op_sel_hi:[0,0,0]
	ds_read_b64_tr_b8 v[146:147], v201 offset:0
	ds_read_b64_tr_b8 v[148:149], v201 offset:0x900
	ds_read_b64_tr_b8 v[150:151], v201 offset:0x1200
	ds_read_b64_tr_b8 v[152:153], v201 offset:0x1b00
	v_mfma_scale_f32_32x32x64_f8f6f4 v[98:113], v[228:235], v[130:137], v[98:113], v219, v218 op_sel_hi:[0,0,0]
	s_nop 15
	s_nop 3
	v_max3_f32 v138, v138, v98, v99
	v_max3_f32 v138, v138, v100, v101
	v_max3_f32 v138, v138, v102, v103
	v_max3_f32 v138, v138, v104, v105
	v_max3_f32 v138, v138, v106, v107
	v_max3_f32 v138, v138, v108, v109
	v_max3_f32 v138, v138, v110, v111
	v_max3_f32 v227, v138, v112, v113
	ds_bpermute_b32 v228, v225, v227
	ds_read_b64_tr_b8 v[138:139], v201 offset:32
	ds_read_b64_tr_b8 v[140:141], v201 offset:0x920
	ds_read_b64_tr_b8 v[142:143], v201 offset:0x1220
	ds_read_b64_tr_b8 v[144:145], v201 offset:0x1b20
	s_waitcnt lgkmcnt(0)
	v_max_f32_e32 v228, v228, v228
	v_max_f32_e32 v227, v227, v228
	v_cmp_lt_f32_e32 vcc, s36, v227
	s_cbranch_vccz .LBB0_1032
	v_add_f32_e32 v67, -4.0, v227
	v_max_f32_e32 v68, 0, v67
	v_exp_f32_e64 v70, -v68
	v_sub_f32_e32 v66, v66, v68
	v_pk_add_f32 v[82:83], v[82:83], v[68:69] op_sel_hi:[1,0] neg_lo:[0,1] neg_hi:[0,1]
	v_pk_add_f32 v[84:85], v[84:85], v[68:69] op_sel_hi:[1,0] neg_lo:[0,1] neg_hi:[0,1]
	v_pk_mul_f32 v[64:65], v[64:65], v[70:71] op_sel_hi:[1,0]
	v_pk_mul_f32 v[62:63], v[62:63], v[70:71] op_sel_hi:[1,0]
	v_pk_mul_f32 v[60:61], v[60:61], v[70:71] op_sel_hi:[1,0]
	v_pk_mul_f32 v[58:59], v[58:59], v[70:71] op_sel_hi:[1,0]
	v_pk_mul_f32 v[56:57], v[56:57], v[70:71] op_sel_hi:[1,0]
	v_pk_mul_f32 v[54:55], v[54:55], v[70:71] op_sel_hi:[1,0]
	v_pk_mul_f32 v[52:53], v[52:53], v[70:71] op_sel_hi:[1,0]
	v_pk_mul_f32 v[50:51], v[50:51], v[70:71] op_sel_hi:[1,0]
	v_pk_mul_f32 v[48:49], v[48:49], v[70:71] op_sel_hi:[1,0]
	v_pk_mul_f32 v[46:47], v[46:47], v[70:71] op_sel_hi:[1,0]
	v_pk_mul_f32 v[44:45], v[44:45], v[70:71] op_sel_hi:[1,0]
	v_pk_mul_f32 v[42:43], v[42:43], v[70:71] op_sel_hi:[1,0]
	v_pk_mul_f32 v[40:41], v[40:41], v[70:71] op_sel_hi:[1,0]
	v_pk_mul_f32 v[38:39], v[38:39], v[70:71] op_sel_hi:[1,0]
	v_pk_mul_f32 v[36:37], v[36:37], v[70:71] op_sel_hi:[1,0]
	v_pk_mul_f32 v[34:35], v[34:35], v[70:71] op_sel_hi:[1,0]
	v_pk_mul_f32 v[32:33], v[32:33], v[70:71] op_sel_hi:[1,0]
	v_pk_mul_f32 v[30:31], v[30:31], v[70:71] op_sel_hi:[1,0]
	v_pk_mul_f32 v[28:29], v[28:29], v[70:71] op_sel_hi:[1,0]
	v_pk_mul_f32 v[26:27], v[26:27], v[70:71] op_sel_hi:[1,0]
	v_pk_mul_f32 v[24:25], v[24:25], v[70:71] op_sel_hi:[1,0]
	v_pk_mul_f32 v[22:23], v[22:23], v[70:71] op_sel_hi:[1,0]
	v_pk_mul_f32 v[20:21], v[20:21], v[70:71] op_sel_hi:[1,0]
	v_pk_mul_f32 v[18:19], v[18:19], v[70:71] op_sel_hi:[1,0]
	v_pk_mul_f32 v[16:17], v[16:17], v[70:71] op_sel_hi:[1,0]
	v_pk_mul_f32 v[14:15], v[14:15], v[70:71] op_sel_hi:[1,0]
	v_pk_mul_f32 v[12:13], v[12:13], v[70:71] op_sel_hi:[1,0]
	v_pk_mul_f32 v[10:11], v[10:11], v[70:71] op_sel_hi:[1,0]
	v_pk_mul_f32 v[8:9], v[8:9], v[70:71] op_sel_hi:[1,0]
	v_pk_mul_f32 v[6:7], v[6:7], v[70:71] op_sel_hi:[1,0]
	v_pk_mul_f32 v[4:5], v[4:5], v[70:71] op_sel_hi:[1,0]
	v_pk_mul_f32 v[2:3], v[2:3], v[70:71] op_sel_hi:[1,0]
	v_pk_add_f32 v[86:87], v[86:87], v[68:69] op_sel_hi:[1,0] neg_lo:[0,1] neg_hi:[0,1]
	v_pk_add_f32 v[88:89], v[88:89], v[68:69] op_sel_hi:[1,0] neg_lo:[0,1] neg_hi:[0,1]
	v_pk_add_f32 v[90:91], v[90:91], v[68:69] op_sel_hi:[1,0] neg_lo:[0,1] neg_hi:[0,1]
	v_pk_add_f32 v[92:93], v[92:93], v[68:69] op_sel_hi:[1,0] neg_lo:[0,1] neg_hi:[0,1]
	v_pk_add_f32 v[94:95], v[94:95], v[68:69] op_sel_hi:[1,0] neg_lo:[0,1] neg_hi:[0,1]
	v_pk_add_f32 v[96:97], v[96:97], v[68:69] op_sel_hi:[1,0] neg_lo:[0,1] neg_hi:[0,1]
	v_pk_add_f32 v[98:99], v[98:99], v[68:69] op_sel_hi:[1,0] neg_lo:[0,1] neg_hi:[0,1]
	v_pk_add_f32 v[100:101], v[100:101], v[68:69] op_sel_hi:[1,0] neg_lo:[0,1] neg_hi:[0,1]
	v_pk_add_f32 v[102:103], v[102:103], v[68:69] op_sel_hi:[1,0] neg_lo:[0,1] neg_hi:[0,1]
	v_pk_add_f32 v[104:105], v[104:105], v[68:69] op_sel_hi:[1,0] neg_lo:[0,1] neg_hi:[0,1]
	v_pk_add_f32 v[106:107], v[106:107], v[68:69] op_sel_hi:[1,0] neg_lo:[0,1] neg_hi:[0,1]
	v_pk_add_f32 v[108:109], v[108:109], v[68:69] op_sel_hi:[1,0] neg_lo:[0,1] neg_hi:[0,1]
	v_pk_add_f32 v[110:111], v[110:111], v[68:69] op_sel_hi:[1,0] neg_lo:[0,1] neg_hi:[0,1]
	v_pk_add_f32 v[112:113], v[112:113], v[68:69] op_sel_hi:[1,0] neg_lo:[0,1] neg_hi:[0,1]
	v_mul_f32_e32 v226, v226, v70
	v_mov_b32_e32 v67, v66
	v_mov_b32_e32 v68, v66
	v_mov_b32_e32 v69, v66
	v_mov_b32_e32 v70, v66
	v_mov_b32_e32 v71, v66
	v_mov_b32_e32 v72, v66
	v_mov_b32_e32 v73, v66
	v_mov_b32_e32 v74, v66
	v_mov_b32_e32 v75, v66
	v_mov_b32_e32 v76, v66
	v_mov_b32_e32 v77, v66
	v_mov_b32_e32 v78, v66
	v_mov_b32_e32 v79, v66
	v_mov_b32_e32 v80, v66
	v_mov_b32_e32 v81, v66
	s_branch .LBB0_1032

.LBB0_1088:
	ds_read_b128 v[84:87], v215 offset:0
	ds_read_b128 v[88:91], v215 offset:16
	ds_read_b128 v[92:95], v215 offset:64
	ds_read_b128 v[96:99], v215 offset:0x50
	ds_read_b128 v[100:103], v215 offset:0x1200
	ds_read_b128 v[104:107], v215 offset:0x1210
	ds_read_b128 v[108:111], v215 offset:0x1240
	ds_read_b128 v[112:115], v215 offset:0x1250
	s_waitcnt lgkmcnt(6)
	v_mfma_scale_f32_32x32x64_f8f6f4 v[116:131], v[84:91], v[148:155], v[68:83], v221, v220 op_sel_hi:[0,0,0]
	s_waitcnt lgkmcnt(4)
	s_waitcnt lgkmcnt(2)
	s_waitcnt lgkmcnt(0)
	ds_read_b64_tr_b8 v[172:173], v214 offset:0
	ds_read_b64_tr_b8 v[174:175], v214 offset:0x900
	ds_read_b64_tr_b8 v[176:177], v214 offset:0x1200
	ds_read_b64_tr_b8 v[178:179], v214 offset:0x1b00
	ds_read_b64_tr_b8 v[164:165], v214 offset:32
	ds_read_b64_tr_b8 v[166:167], v214 offset:0x920
	ds_read_b64_tr_b8 v[168:169], v214 offset:0x1220
	ds_read_b64_tr_b8 v[170:171], v214 offset:0x1b20
	s_mov_b64 s[94:95], -1
	s_and_b64 vcc, exec, s[88:89]
	v_mfma_scale_f32_32x32x64_f8f6f4 v[132:147], v[100:107], v[148:155], v[68:83], v221, v220 op_sel_hi:[0,0,0]
	v_mfma_scale_f32_32x32x64_f8f6f4 v[116:131], v[92:99], v[156:163], v[116:131], v221, v220 op_sel_hi:[0,0,0]
	v_mfma_scale_f32_32x32x64_f8f6f4 v[132:147], v[108:115], v[156:163], v[132:147], v221, v220 op_sel_hi:[0,0,0]
	s_cbranch_vccz .LBB0_1154
	v_lshl_add_u32 v229, s11, 2, v218
	v_mov_b32_e32 v85, 0xf149f2ca
	v_mov_b32_e32 v84, 0xf149f2ca
	s_mov_b64 s[88:89], exec
	v_readlane_b32 s84, v254, 34
	v_readlane_b32 s85, v254, 35
	s_and_b64 s[84:85], s[88:89], s[84:85]
	s_mov_b64 exec, s[84:85]
	s_cbranch_execz .LBB0_1091
	ds_read_b32 v84, v229 offset:18492
	s_waitcnt lgkmcnt(0)
	s_nop 6
	v_fmamk_f32 v84, v84, 0x3fb8aa3b, v116
